# P1 gelu (uc) epilogue rewritten with independent packed ops (same operation order), on top of silu rewrite
# speedup vs baseline: 1.0075x; 1.0017x over previous
; __device__ __forceinline__ float sigmoid_f(float x) { return __builtin_amdgcn_rcpf(1.0f + __builtin_amdgcn_exp2f(-1.4426950408889634f * x)); }
;     template <int ACT, int AUX> __device__ __forceinline__ void run(const f32x4 (&acc)[2][2][4][2], const Unit& uu, int wr, int wc, int fr, int fq) const {
;     ...
;         const int row0 = u.pm * BM + wr * 64 + fr, col0 = u.pn * BM + wc * 32 + 8 * fq;
;         float rsv[8];
; #pragma unroll
;         for (int i = 0; i < 8; ++i) rsv[i] = ss[row0 + (i >> 2) * HALF + (i & 3) * 16];
;         asm volatile("" ::: "memory");
; #pragma unroll
;         for (int i = 0; i < 8; ++i) rsv[i] = __builtin_amdgcn_rsqf(rsv[i] * (1.0f / cfg::DM) + cfg::RMS_EPS);
;         float cs[2][8]; float mx[2][2];
;         if (AUX == 1) {
; #pragma unroll
;             for (int i = 0; i < 16; ++i) cs[i >> 3][i & 7] = 0.f; }
;         if (AUX == 2) { mx[0][0] = mx[0][1] = mx[1][0] = mx[1][1] = 0.f; }
; #pragma unroll
;         for (int ai = 0; ai < 2; ++ai)
; #pragma unroll
;             for (int m = 0; m < 4; ++m) { const int r = row0 + ai * HALF + m * 16; const float rs = rsv[ai * 4 + m];
;                 bf16_t* rowp = O + (size_t)r * cfg::NC + col0; float s1 = 0.f, s2 = 0.f;
; #pragma unroll
;                 for (int bj = 0; bj < 2; ++bj) { f32x4 v0 = acc[ai][bj][m][0] * rs, v1 = acc[ai][bj][m][1] * rs;
; #pragma unroll
;                     for (int j = 0; j < 4; ++j) { v0[j] = act_f<ACT>(v0[j]); v1[j] = act_f<ACT>(v1[j]); }
;                     if (AUX == 4) {
;                         unsigned q[8];
; #pragma unroll
;                         for (int j = 0; j < 4; ++j) { q[j] = (unsigned)fminf(fmaxf(fmaf(v0[j], 255.0f, 0.5f), 1.0f), 255.0f); q[4 + j] = (unsigned)fminf(fmaxf(fmaf(v1[j], 255.0f, 0.5f), 1.0f), 255.0f); }
;                         u32x2 w8; w8.x = q[0] | (q[1] << 8) | (q[2] << 16) | (q[3] << 24); w8.y = q[4] | (q[5] << 8) | (q[6] << 16) | (q[7] << 24);
;                         __builtin_nontemporal_store(w8, (u32x2*)(g8 + ((size_t)((u.pn - 52) >> 4) * cfg::MT + r) * cfg::DM + ((u.pn - 52) & 15) * BM + wc * 32 + 8 * fq + bj * HALF));
;                     } else {
;                     u32x4 w; w.x = cvt_pk_bf16(v0[0], v0[1]); w.y = cvt_pk_bf16(v0[2], v0[3]); w.z = cvt_pk_bf16(v1[0], v1[1]); w.w = cvt_pk_bf16(v1[2], v1[3]);
;                     __builtin_nontemporal_store(w, (u32x4*)(rowp + bj * HALF)); }
.LBB0_189:
	s_and_b64 vcc, exec, s[12:13]
	s_cbranch_vccz .LBB0_207
	s_cmp_gt_i32 s39, 4
	s_mov_b64 s[12:13], -1
	s_cbranch_scc0 .LBB0_205
	s_cmp_gt_i32 s39, 7
	s_cbranch_scc0 .LBB0_193
	v_lshl_add_u32 v148, s2, 8, v1
	v_ashrrev_i32_e32 v149, 31, v148
	s_waitcnt lgkmcnt(0)
	v_lshl_add_u64 v[150:151], v[148:149], 2, s[22:23]
	global_load_dword v152, v[150:151], off
	global_load_dword v154, v[150:151], off offset:64
	global_load_dword v156, v[150:151], off offset:128
	global_load_dword v158, v[150:151], off offset:192
	global_load_dword v160, v[150:151], off offset:512
	global_load_dword v162, v[150:151], off offset:576
	global_load_dword v164, v[150:151], off offset:640
	global_load_dword v166, v[150:151], off offset:704
	v_lshl_or_b32 v174, s1, 8, v191
	v_lshlrev_b32_e32 v174, 1, v174
	v_mov_b32_e32 v175, 0
	s_mov_b32 s41, 0xe800
	v_mov_b64_e32 v[172:173], s[20:21]
	v_mad_i64_i32 v[172:173], s[12:13], v148, s41, v[172:173]
	v_lshl_add_u64 v[172:173], v[172:173], 0, v[174:175]
	s_mov_b32 s100, 0xe8000
	s_mov_b32 s101, 0
	v_mov_b32_e32 v168, 1.0
	v_mov_b32_e32 v170, 0xbfb8aa3b
	v_mov_b32_e32 v148, 0x3d372713
	v_mov_b32_e32 v150, 0x3fcc422a
	s_waitcnt vmcnt(0)
	v_fmamk_f32 v152, v152, 0x39800000, v221
	v_fmamk_f32 v154, v154, 0x39800000, v221
	v_fmamk_f32 v156, v156, 0x39800000, v221
	v_fmamk_f32 v158, v158, 0x39800000, v221
	v_fmamk_f32 v160, v160, 0x39800000, v221
	v_fmamk_f32 v162, v162, 0x39800000, v221
	v_fmamk_f32 v164, v164, 0x39800000, v221
	v_fmamk_f32 v166, v166, 0x39800000, v221
	v_rsq_f32_e32 v152, v152
	v_rsq_f32_e32 v154, v154
	v_rsq_f32_e32 v156, v156
	v_rsq_f32_e32 v158, v158
	v_rsq_f32_e32 v160, v160
	v_rsq_f32_e32 v162, v162
	v_rsq_f32_e32 v164, v164
	v_rsq_f32_e32 v166, v166
	v_pk_mul_f32 v[128:129], v[128:129], v[152:153] op_sel_hi:[1,0]
	v_pk_mul_f32 v[130:131], v[130:131], v[152:153] op_sel_hi:[1,0]
	v_pk_mul_f32 v[124:125], v[124:125], v[152:153] op_sel_hi:[1,0]
	v_pk_mul_f32 v[126:127], v[126:127], v[152:153] op_sel_hi:[1,0]
	v_pk_mul_f32 v[146:147], v[128:129], v[148:149] op_sel_hi:[1,0]
	v_pk_mul_f32 v[176:177], v[130:131], v[148:149] op_sel_hi:[1,0]
	v_pk_mul_f32 v[178:179], v[124:125], v[148:149] op_sel_hi:[1,0]
	v_pk_mul_f32 v[180:181], v[126:127], v[148:149] op_sel_hi:[1,0]
	v_pk_mul_f32 v[146:147], v[128:129], v[146:147]
	v_pk_mul_f32 v[176:177], v[130:131], v[176:177]
	v_pk_mul_f32 v[178:179], v[124:125], v[178:179]
	v_pk_mul_f32 v[180:181], v[126:127], v[180:181]
	v_pk_fma_f32 v[146:147], v[128:129], v[146:147], v[128:129]
	v_pk_fma_f32 v[176:177], v[130:131], v[176:177], v[130:131]
	v_pk_fma_f32 v[178:179], v[124:125], v[178:179], v[124:125]
	v_pk_fma_f32 v[180:181], v[126:127], v[180:181], v[126:127]
	v_pk_mul_f32 v[146:147], v[146:147], v[150:151] op_sel_hi:[1,0]
	v_pk_mul_f32 v[176:177], v[176:177], v[150:151] op_sel_hi:[1,0]
	v_pk_mul_f32 v[178:179], v[178:179], v[150:151] op_sel_hi:[1,0]
	v_pk_mul_f32 v[180:181], v[180:181], v[150:151] op_sel_hi:[1,0]
	v_pk_mul_f32 v[146:147], v[146:147], v[170:171] op_sel_hi:[1,0]
	v_pk_mul_f32 v[176:177], v[176:177], v[170:171] op_sel_hi:[1,0]
	v_pk_mul_f32 v[178:179], v[178:179], v[170:171] op_sel_hi:[1,0]
	v_pk_mul_f32 v[180:181], v[180:181], v[170:171] op_sel_hi:[1,0]
	v_exp_f32_e32 v146, v146
	v_exp_f32_e32 v147, v147
	v_exp_f32_e32 v176, v176
	v_exp_f32_e32 v177, v177
	v_exp_f32_e32 v178, v178
	v_exp_f32_e32 v179, v179
	v_exp_f32_e32 v180, v180
	v_exp_f32_e32 v181, v181
	v_pk_add_f32 v[146:147], v[146:147], v[168:169] op_sel_hi:[1,0]
	v_pk_add_f32 v[176:177], v[176:177], v[168:169] op_sel_hi:[1,0]
	v_pk_add_f32 v[178:179], v[178:179], v[168:169] op_sel_hi:[1,0]
	v_pk_add_f32 v[180:181], v[180:181], v[168:169] op_sel_hi:[1,0]
	v_rcp_f32_e32 v146, v146
	v_rcp_f32_e32 v147, v147
	v_rcp_f32_e32 v176, v176
	v_rcp_f32_e32 v177, v177
	v_rcp_f32_e32 v178, v178
	v_rcp_f32_e32 v179, v179
	v_rcp_f32_e32 v180, v180
	v_rcp_f32_e32 v181, v181
	v_pk_mul_f32 v[128:129], v[128:129], v[146:147]
	v_pk_mul_f32 v[130:131], v[130:131], v[176:177]
	v_pk_mul_f32 v[124:125], v[124:125], v[178:179]
	v_pk_mul_f32 v[126:127], v[126:127], v[180:181]
	v_cvt_pk_bf16_f32 v128, v128, v129
	v_cvt_pk_bf16_f32 v129, v130, v131
	v_cvt_pk_bf16_f32 v130, v124, v125
	v_cvt_pk_bf16_f32 v131, v126, v127
	global_store_dwordx4 v[172:173], v[128:131], off nt
	v_pk_mul_f32 v[120:121], v[120:121], v[152:153] op_sel_hi:[1,0]
	v_pk_mul_f32 v[122:123], v[122:123], v[152:153] op_sel_hi:[1,0]
	v_pk_mul_f32 v[116:117], v[116:117], v[152:153] op_sel_hi:[1,0]
	v_pk_mul_f32 v[118:119], v[118:119], v[152:153] op_sel_hi:[1,0]
	v_pk_mul_f32 v[146:147], v[120:121], v[148:149] op_sel_hi:[1,0]
	v_pk_mul_f32 v[176:177], v[122:123], v[148:149] op_sel_hi:[1,0]
	v_pk_mul_f32 v[178:179], v[116:117], v[148:149] op_sel_hi:[1,0]
	v_pk_mul_f32 v[180:181], v[118:119], v[148:149] op_sel_hi:[1,0]
	v_pk_mul_f32 v[146:147], v[120:121], v[146:147]
	v_pk_mul_f32 v[176:177], v[122:123], v[176:177]
	v_pk_mul_f32 v[178:179], v[116:117], v[178:179]
	v_pk_mul_f32 v[180:181], v[118:119], v[180:181]
	v_pk_fma_f32 v[146:147], v[120:121], v[146:147], v[120:121]
	v_pk_fma_f32 v[176:177], v[122:123], v[176:177], v[122:123]
	v_pk_fma_f32 v[178:179], v[116:117], v[178:179], v[116:117]
	v_pk_fma_f32 v[180:181], v[118:119], v[180:181], v[118:119]
	v_pk_mul_f32 v[146:147], v[146:147], v[150:151] op_sel_hi:[1,0]
	v_pk_mul_f32 v[176:177], v[176:177], v[150:151] op_sel_hi:[1,0]
	v_pk_mul_f32 v[178:179], v[178:179], v[150:151] op_sel_hi:[1,0]
	v_pk_mul_f32 v[180:181], v[180:181], v[150:151] op_sel_hi:[1,0]
	v_pk_mul_f32 v[146:147], v[146:147], v[170:171] op_sel_hi:[1,0]
	v_pk_mul_f32 v[176:177], v[176:177], v[170:171] op_sel_hi:[1,0]
; __device__ __forceinline__ unsigned cvt_pk_bf16(float lo, float hi) { f32x2_t v = {lo, hi}; bf16x2_t b = __builtin_convertvector(v, bf16x2_t); return __builtin_bit_cast(unsigned, b); }
; __device__ __forceinline__ float sigmoid_f(float x) { return __builtin_amdgcn_rcpf(1.0f + __builtin_amdgcn_exp2f(-1.4426950408889634f * x)); }
; template <int ACT> __device__ __forceinline__ float act_f(float v) {
;     if (ACT == 1) return v * sigmoid_f(v);
;     if (ACT == 2) { const float u2 = 1.5957691216057308f * (v + 0.044715f * v * v * v); return v * sigmoid_f(u2); }
;     template <int ACT, int AUX> __device__ __forceinline__ void run(const f32x4 (&acc)[2][2][4][2], const Unit& uu, int wr, int wc, int fr, int fq) const {
;     ...
;             for (int m = 0; m < 4; ++m) { const int r = row0 + ai * HALF + m * 16; const float rs = rsv[ai * 4 + m];
;                 bf16_t* rowp = O + (size_t)r * cfg::NC + col0; float s1 = 0.f, s2 = 0.f;
; #pragma unroll
;                 for (int bj = 0; bj < 2; ++bj) { f32x4 v0 = acc[ai][bj][m][0] * rs, v1 = acc[ai][bj][m][1] * rs;
; #pragma unroll
;                     for (int j = 0; j < 4; ++j) { v0[j] = act_f<ACT>(v0[j]); v1[j] = act_f<ACT>(v1[j]); }
;                     if (AUX == 4) {
;                         unsigned q[8];
; #pragma unroll
;                         for (int j = 0; j < 4; ++j) { q[j] = (unsigned)fminf(fmaxf(fmaf(v0[j], 255.0f, 0.5f), 1.0f), 255.0f); q[4 + j] = (unsigned)fminf(fmaxf(fmaf(v1[j], 255.0f, 0.5f), 1.0f), 255.0f); }
;                         u32x2 w8; w8.x = q[0] | (q[1] << 8) | (q[2] << 16) | (q[3] << 24); w8.y = q[4] | (q[5] << 8) | (q[6] << 16) | (q[7] << 24);
;                         __builtin_nontemporal_store(w8, (u32x2*)(g8 + ((size_t)((u.pn - 52) >> 4) * cfg::MT + r) * cfg::DM + ((u.pn - 52) & 15) * BM + wc * 32 + 8 * fq + bj * HALF));
;                     } else {
;                     u32x4 w; w.x = cvt_pk_bf16(v0[0], v0[1]); w.y = cvt_pk_bf16(v0[2], v0[3]); w.z = cvt_pk_bf16(v1[0], v1[1]); w.w = cvt_pk_bf16(v1[2], v1[3]);
;                     __builtin_nontemporal_store(w, (u32x4*)(rowp + bj * HALF)); }
	v_pk_mul_f32 v[178:179], v[178:179], v[170:171] op_sel_hi:[1,0]
	v_pk_mul_f32 v[180:181], v[180:181], v[170:171] op_sel_hi:[1,0]
	v_exp_f32_e32 v146, v146
	v_exp_f32_e32 v147, v147
	v_exp_f32_e32 v176, v176
	v_exp_f32_e32 v177, v177
	v_exp_f32_e32 v178, v178
	v_exp_f32_e32 v179, v179
	v_exp_f32_e32 v180, v180
	v_exp_f32_e32 v181, v181
	v_pk_add_f32 v[146:147], v[146:147], v[168:169] op_sel_hi:[1,0]
	v_pk_add_f32 v[176:177], v[176:177], v[168:169] op_sel_hi:[1,0]
	v_pk_add_f32 v[178:179], v[178:179], v[168:169] op_sel_hi:[1,0]
	v_pk_add_f32 v[180:181], v[180:181], v[168:169] op_sel_hi:[1,0]
	v_rcp_f32_e32 v146, v146
	v_rcp_f32_e32 v147, v147
	v_rcp_f32_e32 v176, v176
	v_rcp_f32_e32 v177, v177
	v_rcp_f32_e32 v178, v178
	v_rcp_f32_e32 v179, v179
	v_rcp_f32_e32 v180, v180
	v_rcp_f32_e32 v181, v181
	v_pk_mul_f32 v[120:121], v[120:121], v[146:147]
	v_pk_mul_f32 v[122:123], v[122:123], v[176:177]
	v_pk_mul_f32 v[116:117], v[116:117], v[178:179]
	v_pk_mul_f32 v[118:119], v[118:119], v[180:181]
	v_cvt_pk_bf16_f32 v120, v120, v121
	v_cvt_pk_bf16_f32 v121, v122, v123
	v_cvt_pk_bf16_f32 v122, v116, v117
	v_cvt_pk_bf16_f32 v123, v118, v119
	global_store_dwordx4 v[172:173], v[120:123], off offset:256 nt
	v_lshl_add_u64 v[174:175], v[172:173], 0, s[100:101]
	v_pk_mul_f32 v[112:113], v[112:113], v[154:155] op_sel_hi:[1,0]
	v_pk_mul_f32 v[114:115], v[114:115], v[154:155] op_sel_hi:[1,0]
	v_pk_mul_f32 v[108:109], v[108:109], v[154:155] op_sel_hi:[1,0]
	v_pk_mul_f32 v[110:111], v[110:111], v[154:155] op_sel_hi:[1,0]
	v_pk_mul_f32 v[146:147], v[112:113], v[148:149] op_sel_hi:[1,0]
	v_pk_mul_f32 v[176:177], v[114:115], v[148:149] op_sel_hi:[1,0]
	v_pk_mul_f32 v[178:179], v[108:109], v[148:149] op_sel_hi:[1,0]
	v_pk_mul_f32 v[180:181], v[110:111], v[148:149] op_sel_hi:[1,0]
	v_pk_mul_f32 v[146:147], v[112:113], v[146:147]
	v_pk_mul_f32 v[176:177], v[114:115], v[176:177]
	v_pk_mul_f32 v[178:179], v[108:109], v[178:179]
	v_pk_mul_f32 v[180:181], v[110:111], v[180:181]
	v_pk_fma_f32 v[146:147], v[112:113], v[146:147], v[112:113]
	v_pk_fma_f32 v[176:177], v[114:115], v[176:177], v[114:115]
	v_pk_fma_f32 v[178:179], v[108:109], v[178:179], v[108:109]
	v_pk_fma_f32 v[180:181], v[110:111], v[180:181], v[110:111]
	v_pk_mul_f32 v[146:147], v[146:147], v[150:151] op_sel_hi:[1,0]
	v_pk_mul_f32 v[176:177], v[176:177], v[150:151] op_sel_hi:[1,0]
	v_pk_mul_f32 v[178:179], v[178:179], v[150:151] op_sel_hi:[1,0]
	v_pk_mul_f32 v[180:181], v[180:181], v[150:151] op_sel_hi:[1,0]
	v_pk_mul_f32 v[146:147], v[146:147], v[170:171] op_sel_hi:[1,0]
	v_pk_mul_f32 v[176:177], v[176:177], v[170:171] op_sel_hi:[1,0]
	v_pk_mul_f32 v[178:179], v[178:179], v[170:171] op_sel_hi:[1,0]
	v_pk_mul_f32 v[180:181], v[180:181], v[170:171] op_sel_hi:[1,0]
	v_exp_f32_e32 v146, v146
	v_exp_f32_e32 v147, v147
	v_exp_f32_e32 v176, v176
	v_exp_f32_e32 v177, v177
	v_exp_f32_e32 v178, v178
	v_exp_f32_e32 v179, v179
	v_exp_f32_e32 v180, v180
	v_exp_f32_e32 v181, v181
	v_pk_add_f32 v[146:147], v[146:147], v[168:169] op_sel_hi:[1,0]
	v_pk_add_f32 v[176:177], v[176:177], v[168:169] op_sel_hi:[1,0]
	v_pk_add_f32 v[178:179], v[178:179], v[168:169] op_sel_hi:[1,0]
	v_pk_add_f32 v[180:181], v[180:181], v[168:169] op_sel_hi:[1,0]
	v_rcp_f32_e32 v146, v146
	v_rcp_f32_e32 v147, v147
	v_rcp_f32_e32 v176, v176
	v_rcp_f32_e32 v177, v177
	v_rcp_f32_e32 v178, v178
	v_rcp_f32_e32 v179, v179
	v_rcp_f32_e32 v180, v180
	v_rcp_f32_e32 v181, v181
	v_pk_mul_f32 v[112:113], v[112:113], v[146:147]
	v_pk_mul_f32 v[114:115], v[114:115], v[176:177]
	v_pk_mul_f32 v[108:109], v[108:109], v[178:179]
	v_pk_mul_f32 v[110:111], v[110:111], v[180:181]
	v_cvt_pk_bf16_f32 v112, v112, v113
	v_cvt_pk_bf16_f32 v113, v114, v115
	v_cvt_pk_bf16_f32 v114, v108, v109
	v_cvt_pk_bf16_f32 v115, v110, v111
	global_store_dwordx4 v[174:175], v[112:115], off nt
	v_pk_mul_f32 v[104:105], v[104:105], v[154:155] op_sel_hi:[1,0]
	v_pk_mul_f32 v[106:107], v[106:107], v[154:155] op_sel_hi:[1,0]
	v_pk_mul_f32 v[100:101], v[100:101], v[154:155] op_sel_hi:[1,0]
	v_pk_mul_f32 v[102:103], v[102:103], v[154:155] op_sel_hi:[1,0]
	v_pk_mul_f32 v[146:147], v[104:105], v[148:149] op_sel_hi:[1,0]
	v_pk_mul_f32 v[176:177], v[106:107], v[148:149] op_sel_hi:[1,0]
	v_pk_mul_f32 v[178:179], v[100:101], v[148:149] op_sel_hi:[1,0]
	v_pk_mul_f32 v[180:181], v[102:103], v[148:149] op_sel_hi:[1,0]
	v_pk_mul_f32 v[146:147], v[104:105], v[146:147]
	v_pk_mul_f32 v[176:177], v[106:107], v[176:177]
	v_pk_mul_f32 v[178:179], v[100:101], v[178:179]
	v_pk_mul_f32 v[180:181], v[102:103], v[180:181]
	v_pk_fma_f32 v[146:147], v[104:105], v[146:147], v[104:105]
	v_pk_fma_f32 v[176:177], v[106:107], v[176:177], v[106:107]
	v_pk_fma_f32 v[178:179], v[100:101], v[178:179], v[100:101]
	v_pk_fma_f32 v[180:181], v[102:103], v[180:181], v[102:103]
	v_pk_mul_f32 v[146:147], v[146:147], v[150:151] op_sel_hi:[1,0]
	v_pk_mul_f32 v[176:177], v[176:177], v[150:151] op_sel_hi:[1,0]
	v_pk_mul_f32 v[178:179], v[178:179], v[150:151] op_sel_hi:[1,0]
	v_pk_mul_f32 v[180:181], v[180:181], v[150:151] op_sel_hi:[1,0]
	v_pk_mul_f32 v[146:147], v[146:147], v[170:171] op_sel_hi:[1,0]
	v_pk_mul_f32 v[176:177], v[176:177], v[170:171] op_sel_hi:[1,0]
	v_pk_mul_f32 v[178:179], v[178:179], v[170:171] op_sel_hi:[1,0]
	v_pk_mul_f32 v[180:181], v[180:181], v[170:171] op_sel_hi:[1,0]
	v_exp_f32_e32 v146, v146
	v_exp_f32_e32 v147, v147
	v_exp_f32_e32 v176, v176
	v_exp_f32_e32 v177, v177
	v_exp_f32_e32 v178, v178
	v_exp_f32_e32 v179, v179
	v_exp_f32_e32 v180, v180
	v_exp_f32_e32 v181, v181
	v_pk_add_f32 v[146:147], v[146:147], v[168:169] op_sel_hi:[1,0]
	v_pk_add_f32 v[176:177], v[176:177], v[168:169] op_sel_hi:[1,0]
; __device__ __forceinline__ unsigned cvt_pk_bf16(float lo, float hi) { f32x2_t v = {lo, hi}; bf16x2_t b = __builtin_convertvector(v, bf16x2_t); return __builtin_bit_cast(unsigned, b); }
; __device__ __forceinline__ float sigmoid_f(float x) { return __builtin_amdgcn_rcpf(1.0f + __builtin_amdgcn_exp2f(-1.4426950408889634f * x)); }
; template <int ACT> __device__ __forceinline__ float act_f(float v) {
;     if (ACT == 1) return v * sigmoid_f(v);
;     if (ACT == 2) { const float u2 = 1.5957691216057308f * (v + 0.044715f * v * v * v); return v * sigmoid_f(u2); }
;     template <int ACT, int AUX> __device__ __forceinline__ void run(const f32x4 (&acc)[2][2][4][2], const Unit& uu, int wr, int wc, int fr, int fq) const {
;     ...
;             for (int m = 0; m < 4; ++m) { const int r = row0 + ai * HALF + m * 16; const float rs = rsv[ai * 4 + m];
;                 bf16_t* rowp = O + (size_t)r * cfg::NC + col0; float s1 = 0.f, s2 = 0.f;
; #pragma unroll
;                 for (int bj = 0; bj < 2; ++bj) { f32x4 v0 = acc[ai][bj][m][0] * rs, v1 = acc[ai][bj][m][1] * rs;
; #pragma unroll
;                     for (int j = 0; j < 4; ++j) { v0[j] = act_f<ACT>(v0[j]); v1[j] = act_f<ACT>(v1[j]); }
;                     if (AUX == 4) {
;                         unsigned q[8];
; #pragma unroll
;                         for (int j = 0; j < 4; ++j) { q[j] = (unsigned)fminf(fmaxf(fmaf(v0[j], 255.0f, 0.5f), 1.0f), 255.0f); q[4 + j] = (unsigned)fminf(fmaxf(fmaf(v1[j], 255.0f, 0.5f), 1.0f), 255.0f); }
;                         u32x2 w8; w8.x = q[0] | (q[1] << 8) | (q[2] << 16) | (q[3] << 24); w8.y = q[4] | (q[5] << 8) | (q[6] << 16) | (q[7] << 24);
;                         __builtin_nontemporal_store(w8, (u32x2*)(g8 + ((size_t)((u.pn - 52) >> 4) * cfg::MT + r) * cfg::DM + ((u.pn - 52) & 15) * BM + wc * 32 + 8 * fq + bj * HALF));
;                     } else {
;                     u32x4 w; w.x = cvt_pk_bf16(v0[0], v0[1]); w.y = cvt_pk_bf16(v0[2], v0[3]); w.z = cvt_pk_bf16(v1[0], v1[1]); w.w = cvt_pk_bf16(v1[2], v1[3]);
;                     __builtin_nontemporal_store(w, (u32x4*)(rowp + bj * HALF)); }
	v_pk_add_f32 v[178:179], v[178:179], v[168:169] op_sel_hi:[1,0]
	v_pk_add_f32 v[180:181], v[180:181], v[168:169] op_sel_hi:[1,0]
	v_rcp_f32_e32 v146, v146
	v_rcp_f32_e32 v147, v147
	v_rcp_f32_e32 v176, v176
	v_rcp_f32_e32 v177, v177
	v_rcp_f32_e32 v178, v178
	v_rcp_f32_e32 v179, v179
	v_rcp_f32_e32 v180, v180
	v_rcp_f32_e32 v181, v181
	v_pk_mul_f32 v[104:105], v[104:105], v[146:147]
	v_pk_mul_f32 v[106:107], v[106:107], v[176:177]
	v_pk_mul_f32 v[100:101], v[100:101], v[178:179]
	v_pk_mul_f32 v[102:103], v[102:103], v[180:181]
	v_cvt_pk_bf16_f32 v104, v104, v105
	v_cvt_pk_bf16_f32 v105, v106, v107
	v_cvt_pk_bf16_f32 v106, v100, v101
	v_cvt_pk_bf16_f32 v107, v102, v103
	global_store_dwordx4 v[174:175], v[104:107], off offset:256 nt
	v_lshl_add_u64 v[172:173], v[174:175], 0, s[100:101]
	v_pk_mul_f32 v[96:97], v[96:97], v[156:157] op_sel_hi:[1,0]
	v_pk_mul_f32 v[98:99], v[98:99], v[156:157] op_sel_hi:[1,0]
	v_pk_mul_f32 v[92:93], v[92:93], v[156:157] op_sel_hi:[1,0]
	v_pk_mul_f32 v[94:95], v[94:95], v[156:157] op_sel_hi:[1,0]
	v_pk_mul_f32 v[146:147], v[96:97], v[148:149] op_sel_hi:[1,0]
	v_pk_mul_f32 v[176:177], v[98:99], v[148:149] op_sel_hi:[1,0]
	v_pk_mul_f32 v[178:179], v[92:93], v[148:149] op_sel_hi:[1,0]
	v_pk_mul_f32 v[180:181], v[94:95], v[148:149] op_sel_hi:[1,0]
	v_pk_mul_f32 v[146:147], v[96:97], v[146:147]
	v_pk_mul_f32 v[176:177], v[98:99], v[176:177]
	v_pk_mul_f32 v[178:179], v[92:93], v[178:179]
	v_pk_mul_f32 v[180:181], v[94:95], v[180:181]
	v_pk_fma_f32 v[146:147], v[96:97], v[146:147], v[96:97]
	v_pk_fma_f32 v[176:177], v[98:99], v[176:177], v[98:99]
	v_pk_fma_f32 v[178:179], v[92:93], v[178:179], v[92:93]
	v_pk_fma_f32 v[180:181], v[94:95], v[180:181], v[94:95]
	v_pk_mul_f32 v[146:147], v[146:147], v[150:151] op_sel_hi:[1,0]
	v_pk_mul_f32 v[176:177], v[176:177], v[150:151] op_sel_hi:[1,0]
	v_pk_mul_f32 v[178:179], v[178:179], v[150:151] op_sel_hi:[1,0]
	v_pk_mul_f32 v[180:181], v[180:181], v[150:151] op_sel_hi:[1,0]
	v_pk_mul_f32 v[146:147], v[146:147], v[170:171] op_sel_hi:[1,0]
	v_pk_mul_f32 v[176:177], v[176:177], v[170:171] op_sel_hi:[1,0]
	v_pk_mul_f32 v[178:179], v[178:179], v[170:171] op_sel_hi:[1,0]
	v_pk_mul_f32 v[180:181], v[180:181], v[170:171] op_sel_hi:[1,0]
	v_exp_f32_e32 v146, v146
	v_exp_f32_e32 v147, v147
	v_exp_f32_e32 v176, v176
	v_exp_f32_e32 v177, v177
	v_exp_f32_e32 v178, v178
	v_exp_f32_e32 v179, v179
	v_exp_f32_e32 v180, v180
	v_exp_f32_e32 v181, v181
	v_pk_add_f32 v[146:147], v[146:147], v[168:169] op_sel_hi:[1,0]
	v_pk_add_f32 v[176:177], v[176:177], v[168:169] op_sel_hi:[1,0]
	v_pk_add_f32 v[178:179], v[178:179], v[168:169] op_sel_hi:[1,0]
	v_pk_add_f32 v[180:181], v[180:181], v[168:169] op_sel_hi:[1,0]
	v_rcp_f32_e32 v146, v146
	v_rcp_f32_e32 v147, v147
	v_rcp_f32_e32 v176, v176
	v_rcp_f32_e32 v177, v177
	v_rcp_f32_e32 v178, v178
	v_rcp_f32_e32 v179, v179
	v_rcp_f32_e32 v180, v180
	v_rcp_f32_e32 v181, v181
	v_pk_mul_f32 v[96:97], v[96:97], v[146:147]
	v_pk_mul_f32 v[98:99], v[98:99], v[176:177]
	v_pk_mul_f32 v[92:93], v[92:93], v[178:179]
	v_pk_mul_f32 v[94:95], v[94:95], v[180:181]
	v_cvt_pk_bf16_f32 v96, v96, v97
	v_cvt_pk_bf16_f32 v97, v98, v99
	v_cvt_pk_bf16_f32 v98, v92, v93
	v_cvt_pk_bf16_f32 v99, v94, v95
	global_store_dwordx4 v[172:173], v[96:99], off nt
	v_pk_mul_f32 v[88:89], v[88:89], v[156:157] op_sel_hi:[1,0]
	v_pk_mul_f32 v[90:91], v[90:91], v[156:157] op_sel_hi:[1,0]
	v_pk_mul_f32 v[84:85], v[84:85], v[156:157] op_sel_hi:[1,0]
	v_pk_mul_f32 v[86:87], v[86:87], v[156:157] op_sel_hi:[1,0]
	v_pk_mul_f32 v[146:147], v[88:89], v[148:149] op_sel_hi:[1,0]
	v_pk_mul_f32 v[176:177], v[90:91], v[148:149] op_sel_hi:[1,0]
	v_pk_mul_f32 v[178:179], v[84:85], v[148:149] op_sel_hi:[1,0]
	v_pk_mul_f32 v[180:181], v[86:87], v[148:149] op_sel_hi:[1,0]
	v_pk_mul_f32 v[146:147], v[88:89], v[146:147]
	v_pk_mul_f32 v[176:177], v[90:91], v[176:177]
	v_pk_mul_f32 v[178:179], v[84:85], v[178:179]
	v_pk_mul_f32 v[180:181], v[86:87], v[180:181]
	v_pk_fma_f32 v[146:147], v[88:89], v[146:147], v[88:89]
	v_pk_fma_f32 v[176:177], v[90:91], v[176:177], v[90:91]
	v_pk_fma_f32 v[178:179], v[84:85], v[178:179], v[84:85]
	v_pk_fma_f32 v[180:181], v[86:87], v[180:181], v[86:87]
	v_pk_mul_f32 v[146:147], v[146:147], v[150:151] op_sel_hi:[1,0]
	v_pk_mul_f32 v[176:177], v[176:177], v[150:151] op_sel_hi:[1,0]
	v_pk_mul_f32 v[178:179], v[178:179], v[150:151] op_sel_hi:[1,0]
	v_pk_mul_f32 v[180:181], v[180:181], v[150:151] op_sel_hi:[1,0]
	v_pk_mul_f32 v[146:147], v[146:147], v[170:171] op_sel_hi:[1,0]
	v_pk_mul_f32 v[176:177], v[176:177], v[170:171] op_sel_hi:[1,0]
	v_pk_mul_f32 v[178:179], v[178:179], v[170:171] op_sel_hi:[1,0]
	v_pk_mul_f32 v[180:181], v[180:181], v[170:171] op_sel_hi:[1,0]
	v_exp_f32_e32 v146, v146
	v_exp_f32_e32 v147, v147
	v_exp_f32_e32 v176, v176
	v_exp_f32_e32 v177, v177
	v_exp_f32_e32 v178, v178
	v_exp_f32_e32 v179, v179
	v_exp_f32_e32 v180, v180
	v_exp_f32_e32 v181, v181
	v_pk_add_f32 v[146:147], v[146:147], v[168:169] op_sel_hi:[1,0]
	v_pk_add_f32 v[176:177], v[176:177], v[168:169] op_sel_hi:[1,0]
	v_pk_add_f32 v[178:179], v[178:179], v[168:169] op_sel_hi:[1,0]
	v_pk_add_f32 v[180:181], v[180:181], v[168:169] op_sel_hi:[1,0]
	v_rcp_f32_e32 v146, v146
	v_rcp_f32_e32 v147, v147
	v_rcp_f32_e32 v176, v176
	v_rcp_f32_e32 v177, v177
	v_rcp_f32_e32 v178, v178
	v_rcp_f32_e32 v179, v179
	v_rcp_f32_e32 v180, v180
	v_rcp_f32_e32 v181, v181
	v_pk_mul_f32 v[88:89], v[88:89], v[146:147]
	v_pk_mul_f32 v[90:91], v[90:91], v[176:177]
	v_pk_mul_f32 v[84:85], v[84:85], v[178:179]
	v_pk_mul_f32 v[86:87], v[86:87], v[180:181]
	v_cvt_pk_bf16_f32 v88, v88, v89
	v_cvt_pk_bf16_f32 v89, v90, v91
	v_cvt_pk_bf16_f32 v90, v84, v85
; __device__ __forceinline__ unsigned cvt_pk_bf16(float lo, float hi) { f32x2_t v = {lo, hi}; bf16x2_t b = __builtin_convertvector(v, bf16x2_t); return __builtin_bit_cast(unsigned, b); }
; __device__ __forceinline__ float sigmoid_f(float x) { return __builtin_amdgcn_rcpf(1.0f + __builtin_amdgcn_exp2f(-1.4426950408889634f * x)); }
; template <int ACT> __device__ __forceinline__ float act_f(float v) {
;     if (ACT == 1) return v * sigmoid_f(v);
;     if (ACT == 2) { const float u2 = 1.5957691216057308f * (v + 0.044715f * v * v * v); return v * sigmoid_f(u2); }
;     template <int ACT, int AUX> __device__ __forceinline__ void run(const f32x4 (&acc)[2][2][4][2], const Unit& uu, int wr, int wc, int fr, int fq) const {
;     ...
;             for (int m = 0; m < 4; ++m) { const int r = row0 + ai * HALF + m * 16; const float rs = rsv[ai * 4 + m];
;                 bf16_t* rowp = O + (size_t)r * cfg::NC + col0; float s1 = 0.f, s2 = 0.f;
; #pragma unroll
;                 for (int bj = 0; bj < 2; ++bj) { f32x4 v0 = acc[ai][bj][m][0] * rs, v1 = acc[ai][bj][m][1] * rs;
; #pragma unroll
;                     for (int j = 0; j < 4; ++j) { v0[j] = act_f<ACT>(v0[j]); v1[j] = act_f<ACT>(v1[j]); }
;                     if (AUX == 4) {
;                         unsigned q[8];
; #pragma unroll
;                         for (int j = 0; j < 4; ++j) { q[j] = (unsigned)fminf(fmaxf(fmaf(v0[j], 255.0f, 0.5f), 1.0f), 255.0f); q[4 + j] = (unsigned)fminf(fmaxf(fmaf(v1[j], 255.0f, 0.5f), 1.0f), 255.0f); }
;                         u32x2 w8; w8.x = q[0] | (q[1] << 8) | (q[2] << 16) | (q[3] << 24); w8.y = q[4] | (q[5] << 8) | (q[6] << 16) | (q[7] << 24);
;                         __builtin_nontemporal_store(w8, (u32x2*)(g8 + ((size_t)((u.pn - 52) >> 4) * cfg::MT + r) * cfg::DM + ((u.pn - 52) & 15) * BM + wc * 32 + 8 * fq + bj * HALF));
;                     } else {
;                     u32x4 w; w.x = cvt_pk_bf16(v0[0], v0[1]); w.y = cvt_pk_bf16(v0[2], v0[3]); w.z = cvt_pk_bf16(v1[0], v1[1]); w.w = cvt_pk_bf16(v1[2], v1[3]);
;                     __builtin_nontemporal_store(w, (u32x4*)(rowp + bj * HALF)); }
	v_cvt_pk_bf16_f32 v91, v86, v87
	global_store_dwordx4 v[172:173], v[88:91], off offset:256 nt
	v_lshl_add_u64 v[174:175], v[172:173], 0, s[100:101]
	v_pk_mul_f32 v[80:81], v[80:81], v[158:159] op_sel_hi:[1,0]
	v_pk_mul_f32 v[82:83], v[82:83], v[158:159] op_sel_hi:[1,0]
	v_pk_mul_f32 v[76:77], v[76:77], v[158:159] op_sel_hi:[1,0]
	v_pk_mul_f32 v[78:79], v[78:79], v[158:159] op_sel_hi:[1,0]
	v_pk_mul_f32 v[146:147], v[80:81], v[148:149] op_sel_hi:[1,0]
	v_pk_mul_f32 v[176:177], v[82:83], v[148:149] op_sel_hi:[1,0]
	v_pk_mul_f32 v[178:179], v[76:77], v[148:149] op_sel_hi:[1,0]
	v_pk_mul_f32 v[180:181], v[78:79], v[148:149] op_sel_hi:[1,0]
	v_pk_mul_f32 v[146:147], v[80:81], v[146:147]
	v_pk_mul_f32 v[176:177], v[82:83], v[176:177]
	v_pk_mul_f32 v[178:179], v[76:77], v[178:179]
	v_pk_mul_f32 v[180:181], v[78:79], v[180:181]
	v_pk_fma_f32 v[146:147], v[80:81], v[146:147], v[80:81]
	v_pk_fma_f32 v[176:177], v[82:83], v[176:177], v[82:83]
	v_pk_fma_f32 v[178:179], v[76:77], v[178:179], v[76:77]
	v_pk_fma_f32 v[180:181], v[78:79], v[180:181], v[78:79]
	v_pk_mul_f32 v[146:147], v[146:147], v[150:151] op_sel_hi:[1,0]
	v_pk_mul_f32 v[176:177], v[176:177], v[150:151] op_sel_hi:[1,0]
	v_pk_mul_f32 v[178:179], v[178:179], v[150:151] op_sel_hi:[1,0]
	v_pk_mul_f32 v[180:181], v[180:181], v[150:151] op_sel_hi:[1,0]
	v_pk_mul_f32 v[146:147], v[146:147], v[170:171] op_sel_hi:[1,0]
	v_pk_mul_f32 v[176:177], v[176:177], v[170:171] op_sel_hi:[1,0]
	v_pk_mul_f32 v[178:179], v[178:179], v[170:171] op_sel_hi:[1,0]
	v_pk_mul_f32 v[180:181], v[180:181], v[170:171] op_sel_hi:[1,0]
	v_exp_f32_e32 v146, v146
	v_exp_f32_e32 v147, v147
	v_exp_f32_e32 v176, v176
	v_exp_f32_e32 v177, v177
	v_exp_f32_e32 v178, v178
	v_exp_f32_e32 v179, v179
	v_exp_f32_e32 v180, v180
	v_exp_f32_e32 v181, v181
	v_pk_add_f32 v[146:147], v[146:147], v[168:169] op_sel_hi:[1,0]
	v_pk_add_f32 v[176:177], v[176:177], v[168:169] op_sel_hi:[1,0]
	v_pk_add_f32 v[178:179], v[178:179], v[168:169] op_sel_hi:[1,0]
	v_pk_add_f32 v[180:181], v[180:181], v[168:169] op_sel_hi:[1,0]
	v_rcp_f32_e32 v146, v146
	v_rcp_f32_e32 v147, v147
	v_rcp_f32_e32 v176, v176
	v_rcp_f32_e32 v177, v177
	v_rcp_f32_e32 v178, v178
	v_rcp_f32_e32 v179, v179
	v_rcp_f32_e32 v180, v180
	v_rcp_f32_e32 v181, v181
	v_pk_mul_f32 v[80:81], v[80:81], v[146:147]
	v_pk_mul_f32 v[82:83], v[82:83], v[176:177]
	v_pk_mul_f32 v[76:77], v[76:77], v[178:179]
	v_pk_mul_f32 v[78:79], v[78:79], v[180:181]
	v_cvt_pk_bf16_f32 v80, v80, v81
	v_cvt_pk_bf16_f32 v81, v82, v83
	v_cvt_pk_bf16_f32 v82, v76, v77
	v_cvt_pk_bf16_f32 v83, v78, v79
	global_store_dwordx4 v[174:175], v[80:83], off nt
	v_pk_mul_f32 v[72:73], v[72:73], v[158:159] op_sel_hi:[1,0]
	v_pk_mul_f32 v[74:75], v[74:75], v[158:159] op_sel_hi:[1,0]
	v_pk_mul_f32 v[68:69], v[68:69], v[158:159] op_sel_hi:[1,0]
	v_pk_mul_f32 v[70:71], v[70:71], v[158:159] op_sel_hi:[1,0]
	v_pk_mul_f32 v[146:147], v[72:73], v[148:149] op_sel_hi:[1,0]
	v_pk_mul_f32 v[176:177], v[74:75], v[148:149] op_sel_hi:[1,0]
	v_pk_mul_f32 v[178:179], v[68:69], v[148:149] op_sel_hi:[1,0]
	v_pk_mul_f32 v[180:181], v[70:71], v[148:149] op_sel_hi:[1,0]
	v_pk_mul_f32 v[146:147], v[72:73], v[146:147]
	v_pk_mul_f32 v[176:177], v[74:75], v[176:177]
	v_pk_mul_f32 v[178:179], v[68:69], v[178:179]
	v_pk_mul_f32 v[180:181], v[70:71], v[180:181]
	v_pk_fma_f32 v[146:147], v[72:73], v[146:147], v[72:73]
	v_pk_fma_f32 v[176:177], v[74:75], v[176:177], v[74:75]
	v_pk_fma_f32 v[178:179], v[68:69], v[178:179], v[68:69]
	v_pk_fma_f32 v[180:181], v[70:71], v[180:181], v[70:71]
	v_pk_mul_f32 v[146:147], v[146:147], v[150:151] op_sel_hi:[1,0]
	v_pk_mul_f32 v[176:177], v[176:177], v[150:151] op_sel_hi:[1,0]
	v_pk_mul_f32 v[178:179], v[178:179], v[150:151] op_sel_hi:[1,0]
	v_pk_mul_f32 v[180:181], v[180:181], v[150:151] op_sel_hi:[1,0]
	v_pk_mul_f32 v[146:147], v[146:147], v[170:171] op_sel_hi:[1,0]
	v_pk_mul_f32 v[176:177], v[176:177], v[170:171] op_sel_hi:[1,0]
	v_pk_mul_f32 v[178:179], v[178:179], v[170:171] op_sel_hi:[1,0]
	v_pk_mul_f32 v[180:181], v[180:181], v[170:171] op_sel_hi:[1,0]
	v_exp_f32_e32 v146, v146
	v_exp_f32_e32 v147, v147
	v_exp_f32_e32 v176, v176
	v_exp_f32_e32 v177, v177
	v_exp_f32_e32 v178, v178
	v_exp_f32_e32 v179, v179
	v_exp_f32_e32 v180, v180
	v_exp_f32_e32 v181, v181
	v_pk_add_f32 v[146:147], v[146:147], v[168:169] op_sel_hi:[1,0]
	v_pk_add_f32 v[176:177], v[176:177], v[168:169] op_sel_hi:[1,0]
	v_pk_add_f32 v[178:179], v[178:179], v[168:169] op_sel_hi:[1,0]
	v_pk_add_f32 v[180:181], v[180:181], v[168:169] op_sel_hi:[1,0]
	v_rcp_f32_e32 v146, v146
	v_rcp_f32_e32 v147, v147
	v_rcp_f32_e32 v176, v176
	v_rcp_f32_e32 v177, v177
	v_rcp_f32_e32 v178, v178
	v_rcp_f32_e32 v179, v179
	v_rcp_f32_e32 v180, v180
	v_rcp_f32_e32 v181, v181
	v_pk_mul_f32 v[72:73], v[72:73], v[146:147]
	v_pk_mul_f32 v[74:75], v[74:75], v[176:177]
	v_pk_mul_f32 v[68:69], v[68:69], v[178:179]
	v_pk_mul_f32 v[70:71], v[70:71], v[180:181]
	v_cvt_pk_bf16_f32 v72, v72, v73
	v_cvt_pk_bf16_f32 v73, v74, v75
	v_cvt_pk_bf16_f32 v74, v68, v69
	v_cvt_pk_bf16_f32 v75, v70, v71
	global_store_dwordx4 v[174:175], v[72:75], off offset:256 nt
	s_mov_b32 s100, 0x488000
	v_lshl_add_u64 v[172:173], v[174:175], 0, s[100:101]
	s_mov_b32 s100, 0xe8000
	v_pk_mul_f32 v[64:65], v[64:65], v[160:161] op_sel_hi:[1,0]
	v_pk_mul_f32 v[66:67], v[66:67], v[160:161] op_sel_hi:[1,0]
	v_pk_mul_f32 v[60:61], v[60:61], v[160:161] op_sel_hi:[1,0]
	v_pk_mul_f32 v[62:63], v[62:63], v[160:161] op_sel_hi:[1,0]
	v_pk_mul_f32 v[146:147], v[64:65], v[148:149] op_sel_hi:[1,0]
	v_pk_mul_f32 v[176:177], v[66:67], v[148:149] op_sel_hi:[1,0]
	v_pk_mul_f32 v[178:179], v[60:61], v[148:149] op_sel_hi:[1,0]
; __device__ __forceinline__ unsigned cvt_pk_bf16(float lo, float hi) { f32x2_t v = {lo, hi}; bf16x2_t b = __builtin_convertvector(v, bf16x2_t); return __builtin_bit_cast(unsigned, b); }
; __device__ __forceinline__ float sigmoid_f(float x) { return __builtin_amdgcn_rcpf(1.0f + __builtin_amdgcn_exp2f(-1.4426950408889634f * x)); }
; template <int ACT> __device__ __forceinline__ float act_f(float v) {
;     if (ACT == 1) return v * sigmoid_f(v);
;     if (ACT == 2) { const float u2 = 1.5957691216057308f * (v + 0.044715f * v * v * v); return v * sigmoid_f(u2); }
;     template <int ACT, int AUX> __device__ __forceinline__ void run(const f32x4 (&acc)[2][2][4][2], const Unit& uu, int wr, int wc, int fr, int fq) const {
;     ...
;             for (int m = 0; m < 4; ++m) { const int r = row0 + ai * HALF + m * 16; const float rs = rsv[ai * 4 + m];
;                 bf16_t* rowp = O + (size_t)r * cfg::NC + col0; float s1 = 0.f, s2 = 0.f;
; #pragma unroll
;                 for (int bj = 0; bj < 2; ++bj) { f32x4 v0 = acc[ai][bj][m][0] * rs, v1 = acc[ai][bj][m][1] * rs;
; #pragma unroll
;                     for (int j = 0; j < 4; ++j) { v0[j] = act_f<ACT>(v0[j]); v1[j] = act_f<ACT>(v1[j]); }
;                     if (AUX == 4) {
;                         unsigned q[8];
; #pragma unroll
;                         for (int j = 0; j < 4; ++j) { q[j] = (unsigned)fminf(fmaxf(fmaf(v0[j], 255.0f, 0.5f), 1.0f), 255.0f); q[4 + j] = (unsigned)fminf(fmaxf(fmaf(v1[j], 255.0f, 0.5f), 1.0f), 255.0f); }
;                         u32x2 w8; w8.x = q[0] | (q[1] << 8) | (q[2] << 16) | (q[3] << 24); w8.y = q[4] | (q[5] << 8) | (q[6] << 16) | (q[7] << 24);
;                         __builtin_nontemporal_store(w8, (u32x2*)(g8 + ((size_t)((u.pn - 52) >> 4) * cfg::MT + r) * cfg::DM + ((u.pn - 52) & 15) * BM + wc * 32 + 8 * fq + bj * HALF));
;                     } else {
;                     u32x4 w; w.x = cvt_pk_bf16(v0[0], v0[1]); w.y = cvt_pk_bf16(v0[2], v0[3]); w.z = cvt_pk_bf16(v1[0], v1[1]); w.w = cvt_pk_bf16(v1[2], v1[3]);
;                     __builtin_nontemporal_store(w, (u32x4*)(rowp + bj * HALF)); }
	v_pk_mul_f32 v[180:181], v[62:63], v[148:149] op_sel_hi:[1,0]
	v_pk_mul_f32 v[146:147], v[64:65], v[146:147]
	v_pk_mul_f32 v[176:177], v[66:67], v[176:177]
	v_pk_mul_f32 v[178:179], v[60:61], v[178:179]
	v_pk_mul_f32 v[180:181], v[62:63], v[180:181]
	v_pk_fma_f32 v[146:147], v[64:65], v[146:147], v[64:65]
	v_pk_fma_f32 v[176:177], v[66:67], v[176:177], v[66:67]
	v_pk_fma_f32 v[178:179], v[60:61], v[178:179], v[60:61]
	v_pk_fma_f32 v[180:181], v[62:63], v[180:181], v[62:63]
	v_pk_mul_f32 v[146:147], v[146:147], v[150:151] op_sel_hi:[1,0]
	v_pk_mul_f32 v[176:177], v[176:177], v[150:151] op_sel_hi:[1,0]
	v_pk_mul_f32 v[178:179], v[178:179], v[150:151] op_sel_hi:[1,0]
	v_pk_mul_f32 v[180:181], v[180:181], v[150:151] op_sel_hi:[1,0]
	v_pk_mul_f32 v[146:147], v[146:147], v[170:171] op_sel_hi:[1,0]
	v_pk_mul_f32 v[176:177], v[176:177], v[170:171] op_sel_hi:[1,0]
	v_pk_mul_f32 v[178:179], v[178:179], v[170:171] op_sel_hi:[1,0]
	v_pk_mul_f32 v[180:181], v[180:181], v[170:171] op_sel_hi:[1,0]
	v_exp_f32_e32 v146, v146
	v_exp_f32_e32 v147, v147
	v_exp_f32_e32 v176, v176
	v_exp_f32_e32 v177, v177
	v_exp_f32_e32 v178, v178
	v_exp_f32_e32 v179, v179
	v_exp_f32_e32 v180, v180
	v_exp_f32_e32 v181, v181
	v_pk_add_f32 v[146:147], v[146:147], v[168:169] op_sel_hi:[1,0]
	v_pk_add_f32 v[176:177], v[176:177], v[168:169] op_sel_hi:[1,0]
	v_pk_add_f32 v[178:179], v[178:179], v[168:169] op_sel_hi:[1,0]
	v_pk_add_f32 v[180:181], v[180:181], v[168:169] op_sel_hi:[1,0]
	v_rcp_f32_e32 v146, v146
	v_rcp_f32_e32 v147, v147
	v_rcp_f32_e32 v176, v176
	v_rcp_f32_e32 v177, v177
	v_rcp_f32_e32 v178, v178
	v_rcp_f32_e32 v179, v179
	v_rcp_f32_e32 v180, v180
	v_rcp_f32_e32 v181, v181
	v_pk_mul_f32 v[64:65], v[64:65], v[146:147]
	v_pk_mul_f32 v[66:67], v[66:67], v[176:177]
	v_pk_mul_f32 v[60:61], v[60:61], v[178:179]
	v_pk_mul_f32 v[62:63], v[62:63], v[180:181]
	v_cvt_pk_bf16_f32 v64, v64, v65
	v_cvt_pk_bf16_f32 v65, v66, v67
	v_cvt_pk_bf16_f32 v66, v60, v61
	v_cvt_pk_bf16_f32 v67, v62, v63
	global_store_dwordx4 v[172:173], v[64:67], off nt
	v_pk_mul_f32 v[56:57], v[56:57], v[160:161] op_sel_hi:[1,0]
	v_pk_mul_f32 v[58:59], v[58:59], v[160:161] op_sel_hi:[1,0]
	v_pk_mul_f32 v[52:53], v[52:53], v[160:161] op_sel_hi:[1,0]
	v_pk_mul_f32 v[54:55], v[54:55], v[160:161] op_sel_hi:[1,0]
	v_pk_mul_f32 v[146:147], v[56:57], v[148:149] op_sel_hi:[1,0]
	v_pk_mul_f32 v[176:177], v[58:59], v[148:149] op_sel_hi:[1,0]
	v_pk_mul_f32 v[178:179], v[52:53], v[148:149] op_sel_hi:[1,0]
	v_pk_mul_f32 v[180:181], v[54:55], v[148:149] op_sel_hi:[1,0]
	v_pk_mul_f32 v[146:147], v[56:57], v[146:147]
	v_pk_mul_f32 v[176:177], v[58:59], v[176:177]
	v_pk_mul_f32 v[178:179], v[52:53], v[178:179]
	v_pk_mul_f32 v[180:181], v[54:55], v[180:181]
	v_pk_fma_f32 v[146:147], v[56:57], v[146:147], v[56:57]
	v_pk_fma_f32 v[176:177], v[58:59], v[176:177], v[58:59]
	v_pk_fma_f32 v[178:179], v[52:53], v[178:179], v[52:53]
	v_pk_fma_f32 v[180:181], v[54:55], v[180:181], v[54:55]
	v_pk_mul_f32 v[146:147], v[146:147], v[150:151] op_sel_hi:[1,0]
	v_pk_mul_f32 v[176:177], v[176:177], v[150:151] op_sel_hi:[1,0]
	v_pk_mul_f32 v[178:179], v[178:179], v[150:151] op_sel_hi:[1,0]
	v_pk_mul_f32 v[180:181], v[180:181], v[150:151] op_sel_hi:[1,0]
	v_pk_mul_f32 v[146:147], v[146:147], v[170:171] op_sel_hi:[1,0]
	v_pk_mul_f32 v[176:177], v[176:177], v[170:171] op_sel_hi:[1,0]
	v_pk_mul_f32 v[178:179], v[178:179], v[170:171] op_sel_hi:[1,0]
	v_pk_mul_f32 v[180:181], v[180:181], v[170:171] op_sel_hi:[1,0]
	v_exp_f32_e32 v146, v146
	v_exp_f32_e32 v147, v147
	v_exp_f32_e32 v176, v176
	v_exp_f32_e32 v177, v177
	v_exp_f32_e32 v178, v178
	v_exp_f32_e32 v179, v179
	v_exp_f32_e32 v180, v180
	v_exp_f32_e32 v181, v181
	v_pk_add_f32 v[146:147], v[146:147], v[168:169] op_sel_hi:[1,0]
	v_pk_add_f32 v[176:177], v[176:177], v[168:169] op_sel_hi:[1,0]
	v_pk_add_f32 v[178:179], v[178:179], v[168:169] op_sel_hi:[1,0]
	v_pk_add_f32 v[180:181], v[180:181], v[168:169] op_sel_hi:[1,0]
	v_rcp_f32_e32 v146, v146
	v_rcp_f32_e32 v147, v147
	v_rcp_f32_e32 v176, v176
	v_rcp_f32_e32 v177, v177
	v_rcp_f32_e32 v178, v178
	v_rcp_f32_e32 v179, v179
	v_rcp_f32_e32 v180, v180
	v_rcp_f32_e32 v181, v181
	v_pk_mul_f32 v[56:57], v[56:57], v[146:147]
	v_pk_mul_f32 v[58:59], v[58:59], v[176:177]
	v_pk_mul_f32 v[52:53], v[52:53], v[178:179]
	v_pk_mul_f32 v[54:55], v[54:55], v[180:181]
	v_cvt_pk_bf16_f32 v56, v56, v57
	v_cvt_pk_bf16_f32 v57, v58, v59
	v_cvt_pk_bf16_f32 v58, v52, v53
	v_cvt_pk_bf16_f32 v59, v54, v55
	global_store_dwordx4 v[172:173], v[56:59], off offset:256 nt
	v_lshl_add_u64 v[174:175], v[172:173], 0, s[100:101]
	v_pk_mul_f32 v[48:49], v[48:49], v[162:163] op_sel_hi:[1,0]
	v_pk_mul_f32 v[50:51], v[50:51], v[162:163] op_sel_hi:[1,0]
	v_pk_mul_f32 v[44:45], v[44:45], v[162:163] op_sel_hi:[1,0]
	v_pk_mul_f32 v[46:47], v[46:47], v[162:163] op_sel_hi:[1,0]
	v_pk_mul_f32 v[146:147], v[48:49], v[148:149] op_sel_hi:[1,0]
	v_pk_mul_f32 v[176:177], v[50:51], v[148:149] op_sel_hi:[1,0]
	v_pk_mul_f32 v[178:179], v[44:45], v[148:149] op_sel_hi:[1,0]
	v_pk_mul_f32 v[180:181], v[46:47], v[148:149] op_sel_hi:[1,0]
	v_pk_mul_f32 v[146:147], v[48:49], v[146:147]
	v_pk_mul_f32 v[176:177], v[50:51], v[176:177]
	v_pk_mul_f32 v[178:179], v[44:45], v[178:179]
	v_pk_mul_f32 v[180:181], v[46:47], v[180:181]
	v_pk_fma_f32 v[146:147], v[48:49], v[146:147], v[48:49]
	v_pk_fma_f32 v[176:177], v[50:51], v[176:177], v[50:51]
	v_pk_fma_f32 v[178:179], v[44:45], v[178:179], v[44:45]
	v_pk_fma_f32 v[180:181], v[46:47], v[180:181], v[46:47]
	v_pk_mul_f32 v[146:147], v[146:147], v[150:151] op_sel_hi:[1,0]
	v_pk_mul_f32 v[176:177], v[176:177], v[150:151] op_sel_hi:[1,0]
; __device__ __forceinline__ unsigned cvt_pk_bf16(float lo, float hi) { f32x2_t v = {lo, hi}; bf16x2_t b = __builtin_convertvector(v, bf16x2_t); return __builtin_bit_cast(unsigned, b); }
; __device__ __forceinline__ float sigmoid_f(float x) { return __builtin_amdgcn_rcpf(1.0f + __builtin_amdgcn_exp2f(-1.4426950408889634f * x)); }
; template <int ACT> __device__ __forceinline__ float act_f(float v) {
;     if (ACT == 1) return v * sigmoid_f(v);
;     if (ACT == 2) { const float u2 = 1.5957691216057308f * (v + 0.044715f * v * v * v); return v * sigmoid_f(u2); }
;     template <int ACT, int AUX> __device__ __forceinline__ void run(const f32x4 (&acc)[2][2][4][2], const Unit& uu, int wr, int wc, int fr, int fq) const {
;     ...
;             for (int m = 0; m < 4; ++m) { const int r = row0 + ai * HALF + m * 16; const float rs = rsv[ai * 4 + m];
;                 bf16_t* rowp = O + (size_t)r * cfg::NC + col0; float s1 = 0.f, s2 = 0.f;
; #pragma unroll
;                 for (int bj = 0; bj < 2; ++bj) { f32x4 v0 = acc[ai][bj][m][0] * rs, v1 = acc[ai][bj][m][1] * rs;
; #pragma unroll
;                     for (int j = 0; j < 4; ++j) { v0[j] = act_f<ACT>(v0[j]); v1[j] = act_f<ACT>(v1[j]); }
;                     if (AUX == 4) {
;                         unsigned q[8];
; #pragma unroll
;                         for (int j = 0; j < 4; ++j) { q[j] = (unsigned)fminf(fmaxf(fmaf(v0[j], 255.0f, 0.5f), 1.0f), 255.0f); q[4 + j] = (unsigned)fminf(fmaxf(fmaf(v1[j], 255.0f, 0.5f), 1.0f), 255.0f); }
;                         u32x2 w8; w8.x = q[0] | (q[1] << 8) | (q[2] << 16) | (q[3] << 24); w8.y = q[4] | (q[5] << 8) | (q[6] << 16) | (q[7] << 24);
;                         __builtin_nontemporal_store(w8, (u32x2*)(g8 + ((size_t)((u.pn - 52) >> 4) * cfg::MT + r) * cfg::DM + ((u.pn - 52) & 15) * BM + wc * 32 + 8 * fq + bj * HALF));
;                     } else {
;                     u32x4 w; w.x = cvt_pk_bf16(v0[0], v0[1]); w.y = cvt_pk_bf16(v0[2], v0[3]); w.z = cvt_pk_bf16(v1[0], v1[1]); w.w = cvt_pk_bf16(v1[2], v1[3]);
;                     __builtin_nontemporal_store(w, (u32x4*)(rowp + bj * HALF)); }
	v_pk_mul_f32 v[178:179], v[178:179], v[150:151] op_sel_hi:[1,0]
	v_pk_mul_f32 v[180:181], v[180:181], v[150:151] op_sel_hi:[1,0]
	v_pk_mul_f32 v[146:147], v[146:147], v[170:171] op_sel_hi:[1,0]
	v_pk_mul_f32 v[176:177], v[176:177], v[170:171] op_sel_hi:[1,0]
	v_pk_mul_f32 v[178:179], v[178:179], v[170:171] op_sel_hi:[1,0]
	v_pk_mul_f32 v[180:181], v[180:181], v[170:171] op_sel_hi:[1,0]
	v_exp_f32_e32 v146, v146
	v_exp_f32_e32 v147, v147
	v_exp_f32_e32 v176, v176
	v_exp_f32_e32 v177, v177
	v_exp_f32_e32 v178, v178
	v_exp_f32_e32 v179, v179
	v_exp_f32_e32 v180, v180
	v_exp_f32_e32 v181, v181
	v_pk_add_f32 v[146:147], v[146:147], v[168:169] op_sel_hi:[1,0]
	v_pk_add_f32 v[176:177], v[176:177], v[168:169] op_sel_hi:[1,0]
	v_pk_add_f32 v[178:179], v[178:179], v[168:169] op_sel_hi:[1,0]
	v_pk_add_f32 v[180:181], v[180:181], v[168:169] op_sel_hi:[1,0]
	v_rcp_f32_e32 v146, v146
	v_rcp_f32_e32 v147, v147
	v_rcp_f32_e32 v176, v176
	v_rcp_f32_e32 v177, v177
	v_rcp_f32_e32 v178, v178
	v_rcp_f32_e32 v179, v179
	v_rcp_f32_e32 v180, v180
	v_rcp_f32_e32 v181, v181
	v_pk_mul_f32 v[48:49], v[48:49], v[146:147]
	v_pk_mul_f32 v[50:51], v[50:51], v[176:177]
	v_pk_mul_f32 v[44:45], v[44:45], v[178:179]
	v_pk_mul_f32 v[46:47], v[46:47], v[180:181]
	v_cvt_pk_bf16_f32 v48, v48, v49
	v_cvt_pk_bf16_f32 v49, v50, v51
	v_cvt_pk_bf16_f32 v50, v44, v45
	v_cvt_pk_bf16_f32 v51, v46, v47
	global_store_dwordx4 v[174:175], v[48:51], off nt
	v_pk_mul_f32 v[40:41], v[40:41], v[162:163] op_sel_hi:[1,0]
	v_pk_mul_f32 v[42:43], v[42:43], v[162:163] op_sel_hi:[1,0]
	v_pk_mul_f32 v[36:37], v[36:37], v[162:163] op_sel_hi:[1,0]
	v_pk_mul_f32 v[38:39], v[38:39], v[162:163] op_sel_hi:[1,0]
	v_pk_mul_f32 v[146:147], v[40:41], v[148:149] op_sel_hi:[1,0]
	v_pk_mul_f32 v[176:177], v[42:43], v[148:149] op_sel_hi:[1,0]
	v_pk_mul_f32 v[178:179], v[36:37], v[148:149] op_sel_hi:[1,0]
	v_pk_mul_f32 v[180:181], v[38:39], v[148:149] op_sel_hi:[1,0]
	v_pk_mul_f32 v[146:147], v[40:41], v[146:147]
	v_pk_mul_f32 v[176:177], v[42:43], v[176:177]
	v_pk_mul_f32 v[178:179], v[36:37], v[178:179]
	v_pk_mul_f32 v[180:181], v[38:39], v[180:181]
	v_pk_fma_f32 v[146:147], v[40:41], v[146:147], v[40:41]
	v_pk_fma_f32 v[176:177], v[42:43], v[176:177], v[42:43]
	v_pk_fma_f32 v[178:179], v[36:37], v[178:179], v[36:37]
	v_pk_fma_f32 v[180:181], v[38:39], v[180:181], v[38:39]
	v_pk_mul_f32 v[146:147], v[146:147], v[150:151] op_sel_hi:[1,0]
	v_pk_mul_f32 v[176:177], v[176:177], v[150:151] op_sel_hi:[1,0]
	v_pk_mul_f32 v[178:179], v[178:179], v[150:151] op_sel_hi:[1,0]
	v_pk_mul_f32 v[180:181], v[180:181], v[150:151] op_sel_hi:[1,0]
	v_pk_mul_f32 v[146:147], v[146:147], v[170:171] op_sel_hi:[1,0]
	v_pk_mul_f32 v[176:177], v[176:177], v[170:171] op_sel_hi:[1,0]
	v_pk_mul_f32 v[178:179], v[178:179], v[170:171] op_sel_hi:[1,0]
	v_pk_mul_f32 v[180:181], v[180:181], v[170:171] op_sel_hi:[1,0]
	v_exp_f32_e32 v146, v146
	v_exp_f32_e32 v147, v147
	v_exp_f32_e32 v176, v176
	v_exp_f32_e32 v177, v177
	v_exp_f32_e32 v178, v178
	v_exp_f32_e32 v179, v179
	v_exp_f32_e32 v180, v180
	v_exp_f32_e32 v181, v181
	v_pk_add_f32 v[146:147], v[146:147], v[168:169] op_sel_hi:[1,0]
	v_pk_add_f32 v[176:177], v[176:177], v[168:169] op_sel_hi:[1,0]
	v_pk_add_f32 v[178:179], v[178:179], v[168:169] op_sel_hi:[1,0]
	v_pk_add_f32 v[180:181], v[180:181], v[168:169] op_sel_hi:[1,0]
	v_rcp_f32_e32 v146, v146
	v_rcp_f32_e32 v147, v147
	v_rcp_f32_e32 v176, v176
	v_rcp_f32_e32 v177, v177
	v_rcp_f32_e32 v178, v178
	v_rcp_f32_e32 v179, v179
	v_rcp_f32_e32 v180, v180
	v_rcp_f32_e32 v181, v181
	v_pk_mul_f32 v[40:41], v[40:41], v[146:147]
	v_pk_mul_f32 v[42:43], v[42:43], v[176:177]
	v_pk_mul_f32 v[36:37], v[36:37], v[178:179]
	v_pk_mul_f32 v[38:39], v[38:39], v[180:181]
	v_cvt_pk_bf16_f32 v40, v40, v41
	v_cvt_pk_bf16_f32 v41, v42, v43
	v_cvt_pk_bf16_f32 v42, v36, v37
	v_cvt_pk_bf16_f32 v43, v38, v39
	global_store_dwordx4 v[174:175], v[40:43], off offset:256 nt
	v_lshl_add_u64 v[172:173], v[174:175], 0, s[100:101]
	v_pk_mul_f32 v[32:33], v[32:33], v[164:165] op_sel_hi:[1,0]
	v_pk_mul_f32 v[34:35], v[34:35], v[164:165] op_sel_hi:[1,0]
	v_pk_mul_f32 v[28:29], v[28:29], v[164:165] op_sel_hi:[1,0]
	v_pk_mul_f32 v[30:31], v[30:31], v[164:165] op_sel_hi:[1,0]
	v_pk_mul_f32 v[146:147], v[32:33], v[148:149] op_sel_hi:[1,0]
	v_pk_mul_f32 v[176:177], v[34:35], v[148:149] op_sel_hi:[1,0]
	v_pk_mul_f32 v[178:179], v[28:29], v[148:149] op_sel_hi:[1,0]
	v_pk_mul_f32 v[180:181], v[30:31], v[148:149] op_sel_hi:[1,0]
	v_pk_mul_f32 v[146:147], v[32:33], v[146:147]
	v_pk_mul_f32 v[176:177], v[34:35], v[176:177]
	v_pk_mul_f32 v[178:179], v[28:29], v[178:179]
	v_pk_mul_f32 v[180:181], v[30:31], v[180:181]
	v_pk_fma_f32 v[146:147], v[32:33], v[146:147], v[32:33]
	v_pk_fma_f32 v[176:177], v[34:35], v[176:177], v[34:35]
	v_pk_fma_f32 v[178:179], v[28:29], v[178:179], v[28:29]
	v_pk_fma_f32 v[180:181], v[30:31], v[180:181], v[30:31]
	v_pk_mul_f32 v[146:147], v[146:147], v[150:151] op_sel_hi:[1,0]
	v_pk_mul_f32 v[176:177], v[176:177], v[150:151] op_sel_hi:[1,0]
	v_pk_mul_f32 v[178:179], v[178:179], v[150:151] op_sel_hi:[1,0]
	v_pk_mul_f32 v[180:181], v[180:181], v[150:151] op_sel_hi:[1,0]
	v_pk_mul_f32 v[146:147], v[146:147], v[170:171] op_sel_hi:[1,0]
	v_pk_mul_f32 v[176:177], v[176:177], v[170:171] op_sel_hi:[1,0]
	v_pk_mul_f32 v[178:179], v[178:179], v[170:171] op_sel_hi:[1,0]
	v_pk_mul_f32 v[180:181], v[180:181], v[170:171] op_sel_hi:[1,0]
	v_exp_f32_e32 v146, v146
	v_exp_f32_e32 v147, v147
	v_exp_f32_e32 v176, v176
	v_exp_f32_e32 v177, v177
	v_exp_f32_e32 v178, v178
	v_exp_f32_e32 v179, v179
	v_exp_f32_e32 v180, v180
	v_exp_f32_e32 v181, v181
	v_pk_add_f32 v[146:147], v[146:147], v[168:169] op_sel_hi:[1,0]
; __device__ __forceinline__ unsigned cvt_pk_bf16(float lo, float hi) { f32x2_t v = {lo, hi}; bf16x2_t b = __builtin_convertvector(v, bf16x2_t); return __builtin_bit_cast(unsigned, b); }
; __device__ __forceinline__ float sigmoid_f(float x) { return __builtin_amdgcn_rcpf(1.0f + __builtin_amdgcn_exp2f(-1.4426950408889634f * x)); }
; template <int ACT> __device__ __forceinline__ float act_f(float v) {
;     if (ACT == 1) return v * sigmoid_f(v);
;     if (ACT == 2) { const float u2 = 1.5957691216057308f * (v + 0.044715f * v * v * v); return v * sigmoid_f(u2); }
;     template <int ACT, int AUX> __device__ __forceinline__ void run(const f32x4 (&acc)[2][2][4][2], const Unit& uu, int wr, int wc, int fr, int fq) const {
;     ...
;             for (int m = 0; m < 4; ++m) { const int r = row0 + ai * HALF + m * 16; const float rs = rsv[ai * 4 + m];
;                 bf16_t* rowp = O + (size_t)r * cfg::NC + col0; float s1 = 0.f, s2 = 0.f;
; #pragma unroll
;                 for (int bj = 0; bj < 2; ++bj) { f32x4 v0 = acc[ai][bj][m][0] * rs, v1 = acc[ai][bj][m][1] * rs;
; #pragma unroll
;                     for (int j = 0; j < 4; ++j) { v0[j] = act_f<ACT>(v0[j]); v1[j] = act_f<ACT>(v1[j]); }
;                     if (AUX == 4) {
;                         unsigned q[8];
; #pragma unroll
;                         for (int j = 0; j < 4; ++j) { q[j] = (unsigned)fminf(fmaxf(fmaf(v0[j], 255.0f, 0.5f), 1.0f), 255.0f); q[4 + j] = (unsigned)fminf(fmaxf(fmaf(v1[j], 255.0f, 0.5f), 1.0f), 255.0f); }
;                         u32x2 w8; w8.x = q[0] | (q[1] << 8) | (q[2] << 16) | (q[3] << 24); w8.y = q[4] | (q[5] << 8) | (q[6] << 16) | (q[7] << 24);
;                         __builtin_nontemporal_store(w8, (u32x2*)(g8 + ((size_t)((u.pn - 52) >> 4) * cfg::MT + r) * cfg::DM + ((u.pn - 52) & 15) * BM + wc * 32 + 8 * fq + bj * HALF));
;                     } else {
;                     u32x4 w; w.x = cvt_pk_bf16(v0[0], v0[1]); w.y = cvt_pk_bf16(v0[2], v0[3]); w.z = cvt_pk_bf16(v1[0], v1[1]); w.w = cvt_pk_bf16(v1[2], v1[3]);
;                     __builtin_nontemporal_store(w, (u32x4*)(rowp + bj * HALF)); }
	v_pk_add_f32 v[176:177], v[176:177], v[168:169] op_sel_hi:[1,0]
	v_pk_add_f32 v[178:179], v[178:179], v[168:169] op_sel_hi:[1,0]
	v_pk_add_f32 v[180:181], v[180:181], v[168:169] op_sel_hi:[1,0]
	v_rcp_f32_e32 v146, v146
	v_rcp_f32_e32 v147, v147
	v_rcp_f32_e32 v176, v176
	v_rcp_f32_e32 v177, v177
	v_rcp_f32_e32 v178, v178
	v_rcp_f32_e32 v179, v179
	v_rcp_f32_e32 v180, v180
	v_rcp_f32_e32 v181, v181
	v_pk_mul_f32 v[32:33], v[32:33], v[146:147]
	v_pk_mul_f32 v[34:35], v[34:35], v[176:177]
	v_pk_mul_f32 v[28:29], v[28:29], v[178:179]
	v_pk_mul_f32 v[30:31], v[30:31], v[180:181]
	v_cvt_pk_bf16_f32 v32, v32, v33
	v_cvt_pk_bf16_f32 v33, v34, v35
	v_cvt_pk_bf16_f32 v34, v28, v29
	v_cvt_pk_bf16_f32 v35, v30, v31
	global_store_dwordx4 v[172:173], v[32:35], off nt
	v_pk_mul_f32 v[24:25], v[24:25], v[164:165] op_sel_hi:[1,0]
	v_pk_mul_f32 v[26:27], v[26:27], v[164:165] op_sel_hi:[1,0]
	v_pk_mul_f32 v[20:21], v[20:21], v[164:165] op_sel_hi:[1,0]
	v_pk_mul_f32 v[22:23], v[22:23], v[164:165] op_sel_hi:[1,0]
	v_pk_mul_f32 v[146:147], v[24:25], v[148:149] op_sel_hi:[1,0]
	v_pk_mul_f32 v[176:177], v[26:27], v[148:149] op_sel_hi:[1,0]
	v_pk_mul_f32 v[178:179], v[20:21], v[148:149] op_sel_hi:[1,0]
	v_pk_mul_f32 v[180:181], v[22:23], v[148:149] op_sel_hi:[1,0]
	v_pk_mul_f32 v[146:147], v[24:25], v[146:147]
	v_pk_mul_f32 v[176:177], v[26:27], v[176:177]
	v_pk_mul_f32 v[178:179], v[20:21], v[178:179]
	v_pk_mul_f32 v[180:181], v[22:23], v[180:181]
	v_pk_fma_f32 v[146:147], v[24:25], v[146:147], v[24:25]
	v_pk_fma_f32 v[176:177], v[26:27], v[176:177], v[26:27]
	v_pk_fma_f32 v[178:179], v[20:21], v[178:179], v[20:21]
	v_pk_fma_f32 v[180:181], v[22:23], v[180:181], v[22:23]
	v_pk_mul_f32 v[146:147], v[146:147], v[150:151] op_sel_hi:[1,0]
	v_pk_mul_f32 v[176:177], v[176:177], v[150:151] op_sel_hi:[1,0]
	v_pk_mul_f32 v[178:179], v[178:179], v[150:151] op_sel_hi:[1,0]
	v_pk_mul_f32 v[180:181], v[180:181], v[150:151] op_sel_hi:[1,0]
	v_pk_mul_f32 v[146:147], v[146:147], v[170:171] op_sel_hi:[1,0]
	v_pk_mul_f32 v[176:177], v[176:177], v[170:171] op_sel_hi:[1,0]
	v_pk_mul_f32 v[178:179], v[178:179], v[170:171] op_sel_hi:[1,0]
	v_pk_mul_f32 v[180:181], v[180:181], v[170:171] op_sel_hi:[1,0]
	v_exp_f32_e32 v146, v146
	v_exp_f32_e32 v147, v147
	v_exp_f32_e32 v176, v176
	v_exp_f32_e32 v177, v177
	v_exp_f32_e32 v178, v178
	v_exp_f32_e32 v179, v179
	v_exp_f32_e32 v180, v180
	v_exp_f32_e32 v181, v181
	v_pk_add_f32 v[146:147], v[146:147], v[168:169] op_sel_hi:[1,0]
	v_pk_add_f32 v[176:177], v[176:177], v[168:169] op_sel_hi:[1,0]
	v_pk_add_f32 v[178:179], v[178:179], v[168:169] op_sel_hi:[1,0]
	v_pk_add_f32 v[180:181], v[180:181], v[168:169] op_sel_hi:[1,0]
	v_rcp_f32_e32 v146, v146
	v_rcp_f32_e32 v147, v147
	v_rcp_f32_e32 v176, v176
	v_rcp_f32_e32 v177, v177
	v_rcp_f32_e32 v178, v178
	v_rcp_f32_e32 v179, v179
	v_rcp_f32_e32 v180, v180
	v_rcp_f32_e32 v181, v181
	v_pk_mul_f32 v[24:25], v[24:25], v[146:147]
	v_pk_mul_f32 v[26:27], v[26:27], v[176:177]
	v_pk_mul_f32 v[20:21], v[20:21], v[178:179]
	v_pk_mul_f32 v[22:23], v[22:23], v[180:181]
	v_cvt_pk_bf16_f32 v24, v24, v25
	v_cvt_pk_bf16_f32 v25, v26, v27
	v_cvt_pk_bf16_f32 v26, v20, v21
	v_cvt_pk_bf16_f32 v27, v22, v23
	global_store_dwordx4 v[172:173], v[24:27], off offset:256 nt
	v_lshl_add_u64 v[174:175], v[172:173], 0, s[100:101]
	v_pk_mul_f32 v[16:17], v[16:17], v[166:167] op_sel_hi:[1,0]
	v_pk_mul_f32 v[18:19], v[18:19], v[166:167] op_sel_hi:[1,0]
	v_pk_mul_f32 v[12:13], v[12:13], v[166:167] op_sel_hi:[1,0]
	v_pk_mul_f32 v[14:15], v[14:15], v[166:167] op_sel_hi:[1,0]
	v_pk_mul_f32 v[146:147], v[16:17], v[148:149] op_sel_hi:[1,0]
	v_pk_mul_f32 v[176:177], v[18:19], v[148:149] op_sel_hi:[1,0]
	v_pk_mul_f32 v[178:179], v[12:13], v[148:149] op_sel_hi:[1,0]
	v_pk_mul_f32 v[180:181], v[14:15], v[148:149] op_sel_hi:[1,0]
	v_pk_mul_f32 v[146:147], v[16:17], v[146:147]
	v_pk_mul_f32 v[176:177], v[18:19], v[176:177]
	v_pk_mul_f32 v[178:179], v[12:13], v[178:179]
	v_pk_mul_f32 v[180:181], v[14:15], v[180:181]
	v_pk_fma_f32 v[146:147], v[16:17], v[146:147], v[16:17]
	v_pk_fma_f32 v[176:177], v[18:19], v[176:177], v[18:19]
; __device__ __forceinline__ unsigned cvt_pk_bf16(float lo, float hi) { f32x2_t v = {lo, hi}; bf16x2_t b = __builtin_convertvector(v, bf16x2_t); return __builtin_bit_cast(unsigned, b); }
; __device__ __forceinline__ float sigmoid_f(float x) { return __builtin_amdgcn_rcpf(1.0f + __builtin_amdgcn_exp2f(-1.4426950408889634f * x)); }
; template <int ACT> __device__ __forceinline__ float act_f(float v) {
;     if (ACT == 1) return v * sigmoid_f(v);
;     if (ACT == 2) { const float u2 = 1.5957691216057308f * (v + 0.044715f * v * v * v); return v * sigmoid_f(u2); }
;     template <int ACT, int AUX> __device__ __forceinline__ void run(const f32x4 (&acc)[2][2][4][2], const Unit& uu, int wr, int wc, int fr, int fq) const {
;     ...
;             for (int m = 0; m < 4; ++m) { const int r = row0 + ai * HALF + m * 16; const float rs = rsv[ai * 4 + m];
;                 bf16_t* rowp = O + (size_t)r * cfg::NC + col0; float s1 = 0.f, s2 = 0.f;
; #pragma unroll
;                 for (int bj = 0; bj < 2; ++bj) { f32x4 v0 = acc[ai][bj][m][0] * rs, v1 = acc[ai][bj][m][1] * rs;
; #pragma unroll
;                     for (int j = 0; j < 4; ++j) { v0[j] = act_f<ACT>(v0[j]); v1[j] = act_f<ACT>(v1[j]); }
;                     if (AUX == 4) {
;                         unsigned q[8];
; #pragma unroll
;                         for (int j = 0; j < 4; ++j) { q[j] = (unsigned)fminf(fmaxf(fmaf(v0[j], 255.0f, 0.5f), 1.0f), 255.0f); q[4 + j] = (unsigned)fminf(fmaxf(fmaf(v1[j], 255.0f, 0.5f), 1.0f), 255.0f); }
;                         u32x2 w8; w8.x = q[0] | (q[1] << 8) | (q[2] << 16) | (q[3] << 24); w8.y = q[4] | (q[5] << 8) | (q[6] << 16) | (q[7] << 24);
;                         __builtin_nontemporal_store(w8, (u32x2*)(g8 + ((size_t)((u.pn - 52) >> 4) * cfg::MT + r) * cfg::DM + ((u.pn - 52) & 15) * BM + wc * 32 + 8 * fq + bj * HALF));
;                     } else {
;                     u32x4 w; w.x = cvt_pk_bf16(v0[0], v0[1]); w.y = cvt_pk_bf16(v0[2], v0[3]); w.z = cvt_pk_bf16(v1[0], v1[1]); w.w = cvt_pk_bf16(v1[2], v1[3]);
;                     __builtin_nontemporal_store(w, (u32x4*)(rowp + bj * HALF)); }
	v_pk_fma_f32 v[178:179], v[12:13], v[178:179], v[12:13]
	v_pk_fma_f32 v[180:181], v[14:15], v[180:181], v[14:15]
	v_pk_mul_f32 v[146:147], v[146:147], v[150:151] op_sel_hi:[1,0]
	v_pk_mul_f32 v[176:177], v[176:177], v[150:151] op_sel_hi:[1,0]
	v_pk_mul_f32 v[178:179], v[178:179], v[150:151] op_sel_hi:[1,0]
	v_pk_mul_f32 v[180:181], v[180:181], v[150:151] op_sel_hi:[1,0]
	v_pk_mul_f32 v[146:147], v[146:147], v[170:171] op_sel_hi:[1,0]
	v_pk_mul_f32 v[176:177], v[176:177], v[170:171] op_sel_hi:[1,0]
	v_pk_mul_f32 v[178:179], v[178:179], v[170:171] op_sel_hi:[1,0]
	v_pk_mul_f32 v[180:181], v[180:181], v[170:171] op_sel_hi:[1,0]
	v_exp_f32_e32 v146, v146
	v_exp_f32_e32 v147, v147
	v_exp_f32_e32 v176, v176
	v_exp_f32_e32 v177, v177
	v_exp_f32_e32 v178, v178
	v_exp_f32_e32 v179, v179
	v_exp_f32_e32 v180, v180
	v_exp_f32_e32 v181, v181
	v_pk_add_f32 v[146:147], v[146:147], v[168:169] op_sel_hi:[1,0]
	v_pk_add_f32 v[176:177], v[176:177], v[168:169] op_sel_hi:[1,0]
	v_pk_add_f32 v[178:179], v[178:179], v[168:169] op_sel_hi:[1,0]
	v_pk_add_f32 v[180:181], v[180:181], v[168:169] op_sel_hi:[1,0]
	v_rcp_f32_e32 v146, v146
	v_rcp_f32_e32 v147, v147
	v_rcp_f32_e32 v176, v176
	v_rcp_f32_e32 v177, v177
	v_rcp_f32_e32 v178, v178
	v_rcp_f32_e32 v179, v179
	v_rcp_f32_e32 v180, v180
	v_rcp_f32_e32 v181, v181
	v_pk_mul_f32 v[16:17], v[16:17], v[146:147]
	v_pk_mul_f32 v[18:19], v[18:19], v[176:177]
	v_pk_mul_f32 v[12:13], v[12:13], v[178:179]
	v_pk_mul_f32 v[14:15], v[14:15], v[180:181]
	v_cvt_pk_bf16_f32 v16, v16, v17
	v_cvt_pk_bf16_f32 v17, v18, v19
	v_cvt_pk_bf16_f32 v18, v12, v13
	v_cvt_pk_bf16_f32 v19, v14, v15
	global_store_dwordx4 v[174:175], v[16:19], off nt
	v_pk_mul_f32 v[8:9], v[8:9], v[166:167] op_sel_hi:[1,0]
	v_pk_mul_f32 v[10:11], v[10:11], v[166:167] op_sel_hi:[1,0]
	v_pk_mul_f32 v[4:5], v[4:5], v[166:167] op_sel_hi:[1,0]
	v_pk_mul_f32 v[6:7], v[6:7], v[166:167] op_sel_hi:[1,0]
	v_pk_mul_f32 v[146:147], v[8:9], v[148:149] op_sel_hi:[1,0]
	v_pk_mul_f32 v[176:177], v[10:11], v[148:149] op_sel_hi:[1,0]
	v_pk_mul_f32 v[178:179], v[4:5], v[148:149] op_sel_hi:[1,0]
	v_pk_mul_f32 v[180:181], v[6:7], v[148:149] op_sel_hi:[1,0]
	v_pk_mul_f32 v[146:147], v[8:9], v[146:147]
	v_pk_mul_f32 v[176:177], v[10:11], v[176:177]
	v_pk_mul_f32 v[178:179], v[4:5], v[178:179]
	v_pk_mul_f32 v[180:181], v[6:7], v[180:181]
	v_pk_fma_f32 v[146:147], v[8:9], v[146:147], v[8:9]
	v_pk_fma_f32 v[176:177], v[10:11], v[176:177], v[10:11]
	v_pk_fma_f32 v[178:179], v[4:5], v[178:179], v[4:5]
	v_pk_fma_f32 v[180:181], v[6:7], v[180:181], v[6:7]
	v_pk_mul_f32 v[146:147], v[146:147], v[150:151] op_sel_hi:[1,0]
	v_pk_mul_f32 v[176:177], v[176:177], v[150:151] op_sel_hi:[1,0]
	v_pk_mul_f32 v[178:179], v[178:179], v[150:151] op_sel_hi:[1,0]
	v_pk_mul_f32 v[180:181], v[180:181], v[150:151] op_sel_hi:[1,0]
	v_pk_mul_f32 v[146:147], v[146:147], v[170:171] op_sel_hi:[1,0]
	v_pk_mul_f32 v[176:177], v[176:177], v[170:171] op_sel_hi:[1,0]
	v_pk_mul_f32 v[178:179], v[178:179], v[170:171] op_sel_hi:[1,0]
	v_pk_mul_f32 v[180:181], v[180:181], v[170:171] op_sel_hi:[1,0]
	v_exp_f32_e32 v146, v146
	v_exp_f32_e32 v147, v147
	v_exp_f32_e32 v176, v176
	v_exp_f32_e32 v177, v177
	v_exp_f32_e32 v178, v178
	v_exp_f32_e32 v179, v179
	v_exp_f32_e32 v180, v180
	v_exp_f32_e32 v181, v181
	v_pk_add_f32 v[146:147], v[146:147], v[168:169] op_sel_hi:[1,0]
	v_pk_add_f32 v[176:177], v[176:177], v[168:169] op_sel_hi:[1,0]
	v_pk_add_f32 v[178:179], v[178:179], v[168:169] op_sel_hi:[1,0]
	v_pk_add_f32 v[180:181], v[180:181], v[168:169] op_sel_hi:[1,0]
	v_rcp_f32_e32 v146, v146
	v_rcp_f32_e32 v147, v147
	v_rcp_f32_e32 v176, v176
	v_rcp_f32_e32 v177, v177
	v_rcp_f32_e32 v178, v178
	v_rcp_f32_e32 v179, v179
	v_rcp_f32_e32 v180, v180
	v_rcp_f32_e32 v181, v181
	v_pk_mul_f32 v[8:9], v[8:9], v[146:147]
	v_pk_mul_f32 v[10:11], v[10:11], v[176:177]
	v_pk_mul_f32 v[4:5], v[4:5], v[178:179]
	v_pk_mul_f32 v[6:7], v[6:7], v[180:181]
	v_cvt_pk_bf16_f32 v8, v8, v9
	v_cvt_pk_bf16_f32 v9, v10, v11
	v_cvt_pk_bf16_f32 v10, v4, v5
	v_cvt_pk_bf16_f32 v11, v6, v7
	global_store_dwordx4 v[174:175], v[8:11], off offset:256 nt
	s_mov_b64 s[12:13], 0
